# MoE GEMM tile heads: tile->expert entry via (cached) scalar load, so the tile boundary no longer drains the previous tile's epilogue stores with vmcnt(0)
# speedup vs baseline: 1.0210x; 1.0210x over previous
;     __device__ bool next(int i, Unit& u) const { if (i > 0 || c >= 16) return false; u.pm = c; u.pn = 0; u.be = c >> 3; return true; }
;     __device__ bool next(int i, Unit& u) const {
;         const long L = (long)i * G + c; if (L >= nwg) return false;
;         static_map((int)L, nM, nN, u.pm, u.pn); u.be = __builtin_amdgcn_readfirstlane(tile_e[u.pm]); return true;
;     }
.LBB0_1094:
	s_add_i32 s54, s54, 1
	v_readlane_b32 s0, v252, 38
	v_readlane_b32 s4, v252, 37
	s_mul_i32 s0, s54, s0
	s_mul_hi_u32 s1, s54, s4
	s_add_i32 s1, s1, s0
	s_mul_i32 s0, s54, s4
	v_readlane_b32 s4, v254, 40
	v_readlane_b32 s5, v254, 41
	s_add_u32 s0, s0, s4
	s_addc_u32 s1, s1, s5
	v_mov_b64_e32 v[2:3], s[6:7]
	v_cmp_ge_i64_e32 vcc, s[0:1], v[2:3]
	v_cmp_lt_i64_e64 s[4:5], s[0:1], v[2:3]
	s_mov_b64 s[20:21], s[10:11]
	s_cbranch_vccnz .LBB0_1096
	s_ashr_i32 s1, s0, 31
	s_lshr_b32 s1, s1, 29
	s_add_i32 s1, s0, s1
	s_ashr_i32 s14, s1, 3
	s_and_b32 s1, s1, -8
	s_sub_i32 s0, s0, s1
	s_cmp_lt_i32 s0, 0
	s_cselect_b32 s1, s49, s48
	s_mul_i32 s0, s0, s1
	s_add_i32 s0, s0, s14
	s_mul_hi_i32 s1, s0, 0x92492493
	s_add_i32 s1, s1, s0
	s_lshr_b32 s14, s1, 31
	s_ashr_i32 s1, s1, 8
	s_add_i32 s1, s1, s14
	s_lshl_b32 s14, s1, 3
	s_sub_i32 s15, s28, s14
	s_min_i32 s15, s15, 8
	s_abs_i32 s16, s15
	v_cvt_f32_u32_e32 v2, s16
	s_sub_i32 s18, 0, s16
	s_mulk_i32 s1, 0x1c0
	s_sub_i32 s0, s0, s1
	v_rcp_iflag_f32_e32 v2, v2
	s_abs_i32 s1, s0
	s_xor_b32 s17, s0, s15
	s_ashr_i32 s17, s17, 31
	v_mul_f32_e32 v2, 0x4f7ffffe, v2
	v_cvt_u32_f32_e32 v2, v2
	s_nop 0
	v_readfirstlane_b32 s19, v2
	s_mul_i32 s18, s18, s19
	s_mul_hi_u32 s18, s19, s18
	s_add_i32 s19, s19, s18
	s_mul_hi_u32 s18, s1, s19
	s_mul_i32 s19, s18, s16
	s_sub_i32 s1, s1, s19
	s_add_i32 s20, s18, 1
	s_sub_i32 s19, s1, s16
	s_cmp_ge_u32 s1, s16
	s_cselect_b32 s18, s20, s18
	s_cselect_b32 s1, s19, s1
	s_add_i32 s19, s18, 1
	s_cmp_ge_u32 s1, s16
	s_cselect_b32 s1, s19, s18
	s_xor_b32 s1, s1, s17
	s_sub_i32 s16, s1, s17
	s_mul_i32 s1, s16, s15
	s_sub_i32 s0, s0, s1
	s_add_i32 s18, s14, s0
	s_ashr_i32 s19, s18, 31
	s_lshl_b64 s[0:1], s[18:19], 2
	v_readlane_b32 s14, v252, 25
	s_add_u32 s0, s14, s0
	v_readlane_b32 s14, v252, 26
	s_addc_u32 s1, s14, s1
	s_load_dword s55, s[0:1], 0x0
	s_mov_b64 s[20:21], -1
	s_waitcnt lgkmcnt(0)

;     __device__ bool next(int i, Unit& u) const { if (i > 0 || c >= 16) return false; u.pm = c; u.pn = 0; u.be = c >> 3; return true; }
;     __device__ bool next(int i, Unit& u) const {
;         const long L = (long)i * G + c; if (L >= nwg) return false;
;         int v, pn; static_map((int)L, nV, nN, v, pn); const int h = v >= nT ? 1 : 0, t = v - h * nT;
;         u.pm = h * MAXPT + t; u.pn = pn; u.be = __builtin_amdgcn_readfirstlane(tile_e[t]) * 2 + h; return true;
;     }
.LBB0_1255:
	s_add_i32 s50, s50, 1
	v_readlane_b32 s0, v252, 10
	s_mul_i32 s0, s50, s0
	s_mul_hi_u32 s1, s50, s33
	s_add_i32 s1, s1, s0
	s_mul_i32 s0, s50, s33
	v_readlane_b32 s4, v254, 40
	v_readlane_b32 s5, v254, 41
	s_add_u32 s0, s0, s4
	s_addc_u32 s1, s1, s5
	v_mov_b64_e32 v[2:3], s[6:7]
	v_cmp_ge_i64_e32 vcc, s[0:1], v[2:3]
	v_cmp_lt_i64_e64 s[4:5], s[0:1], v[2:3]
	s_cbranch_vccnz .LBB0_1257
	s_ashr_i32 s1, s0, 31
	s_lshr_b32 s1, s1, 29
	s_add_i32 s1, s0, s1
	s_ashr_i32 s12, s1, 3
	s_and_b32 s1, s1, -8
	s_sub_i32 s0, s0, s1
	s_cmp_lt_i32 s0, 0
	s_cselect_b32 s1, s41, s31
	s_mul_i32 s0, s0, s1
	s_add_i32 s0, s0, s12
	s_ashr_i32 s1, s0, 31
	s_lshr_b32 s1, s1, 26
	s_add_i32 s1, s0, s1
	s_ashr_i32 s12, s1, 6
	s_lshl_b32 s12, s12, 3
	s_sub_i32 s13, s31, s12
	s_min_i32 s13, s13, 8
	s_abs_i32 s14, s13
	v_cvt_f32_u32_e32 v2, s14
	s_sub_i32 s20, 0, s14
	s_andn2_b32 s1, s1, 63
	s_sub_i32 s0, s0, s1
	v_rcp_iflag_f32_e32 v2, v2
	s_abs_i32 s1, s0
	s_xor_b32 s15, s0, s13
	s_ashr_i32 s15, s15, 31
	v_mul_f32_e32 v2, 0x4f7ffffe, v2
	v_cvt_u32_f32_e32 v2, v2
	s_nop 0
	v_readfirstlane_b32 s21, v2
	s_mul_i32 s20, s20, s21
	s_mul_hi_u32 s20, s21, s20
	s_add_i32 s21, s21, s20
	s_mul_hi_u32 s20, s1, s21
	s_mul_i32 s21, s20, s14
	s_sub_i32 s1, s1, s21
	s_add_i32 s22, s20, 1
	s_sub_i32 s21, s1, s14
	s_cmp_ge_u32 s1, s14
	s_cselect_b32 s20, s22, s20
	s_cselect_b32 s1, s21, s1
	s_add_i32 s21, s20, 1
	s_cmp_ge_u32 s1, s14
	s_cselect_b32 s1, s21, s20
	s_xor_b32 s1, s1, s15
	s_sub_i32 s51, s1, s15
	s_mul_i32 s1, s51, s13
	s_sub_i32 s0, s0, s1
	s_add_i32 s12, s12, s0
	s_cmp_ge_i32 s12, s28
	s_cselect_b64 s[0:1], -1, 0
	v_cndmask_b32_e64 v2, 0, 1, s[0:1]
	s_and_b64 s[0:1], s[0:1], exec
	s_cselect_b32 s0, s28, 0
	s_cselect_b32 s1, 0x48, 0
	s_sub_i32 s0, s12, s0
	s_add_i32 s52, s0, s1
	s_ashr_i32 s1, s0, 31
	s_lshl_b64 s[0:1], s[0:1], 2
	v_readlane_b32 s12, v252, 25
	s_add_u32 s0, s12, s0
	v_readlane_b32 s12, v252, 26
	s_addc_u32 s1, s12, s1
	s_load_dword s12, s[0:1], 0x0
	s_waitcnt lgkmcnt(0)
	v_readfirstlane_b32 s1, v2
	s_lshl_b32 s0, s12, 1
	s_or_b32 s53, s0, s1
